# v23 + diff SGPR-base DMA blocks reordered (m0 write first) so the s_nop pads are gone
# baseline (speedup 1.0000x reference)
; #define DMA_WAIT(last) do { if (last) asm volatile("s_waitcnt vmcnt(0)" ::: "memory"); else asm volatile("s_waitcnt vmcnt(%0)" :: "n"(NPW) : "memory"); } while (0)
; template <int DK, int DV, bool OFF, class QLoader> ...
;     ...
;   f32x16 pA0, pA1, pB0, pB1; bf16x8 pa0, pa1, pa2, pa3; const int NT = nkeys / KVBLK;
;   DMA_TILE(0, 0); DMA_TILE(1, 1); DMA_WAIT(false); __syncthreads(); if (2 < NT) DMA_TILE(2, 2);
;   qkt<DK>(pA0, pA1, K_lds, qr, r32, hi); partialSM<DK, OFF>(pA0, pA1, negMC);
.LBB0_859:
.LBB0_861:
	s_add_i32 s26, s55, -2
	s_cmp_ge_u32 s26, s95
	s_waitcnt vmcnt(0)
	s_barrier
	s_cbranch_scc1 .LBB0_863
	s_cmp_lg_u32 s80, 0
	s_cbranch_scc1 .LBB0_863
	s_mov_b32 m0, s81
	s_add_u32 s98, s76, 0x1ec08000
	s_addc_u32 s99, s77, 0
	global_load_lds_dwordx4 v0, s[98:99]
	s_mov_b32 m0, s82
	s_add_u32 s98, s78, 0xdc01000
	s_addc_u32 s99, s79, 0
	global_load_lds_dwordx4 v232, s[98:99]
	s_mov_b32 m0, s84
	s_add_u32 s98, s98, 0x80
	s_addc_u32 s99, s99, 0
	global_load_lds_dwordx4 v232, s[98:99]
.LBB0_863:
	ds_read_b128 v[66:69], v162 offset:32768
	ds_read_b128 v[70:73], v162 offset:36864
	ds_read_b128 v[130:133], v164 offset:32768
	ds_read_b128 v[134:137], v164 offset:36864
	v_exp_f32_e32 v82, v82
	v_add_f32_e32 v180, 0, v197
	v_add_f32_e32 v180, v200, v180
	v_add_f32_e32 v180, v198, v180
	v_add_f32_e32 v180, v202, v180
	v_add_f32_e32 v180, v204, v180
	v_add_f32_e32 v180, v207, v180
	v_add_f32_e32 v180, v205, v180
	v_add_f32_e32 v180, v210, v180
	v_add_f32_e32 v180, v199, v180
	v_add_f32_e32 v180, v203, v180
	v_add_f32_e32 v180, v201, v180
	v_add_f32_e32 v180, v209, v180
	v_add_f32_e32 v180, v206, v180
	v_add_f32_e32 v180, v211, v180
	v_add_f32_e32 v180, v208, v180
	v_add_f32_e32 v180, v212, v180
	s_waitcnt lgkmcnt(0)
	v_mfma_f32_32x32x16_bf16 v[98:113], v[66:69], v[114:117], 0
	v_exp_f32_e32 v83, v83
	v_exp_f32_e32 v84, v84
	v_exp_f32_e32 v85, v85
	v_exp_f32_e32 v86, v86
	v_exp_f32_e32 v87, v87
	v_exp_f32_e32 v88, v88
	v_exp_f32_e32 v89, v89
	v_mfma_f32_32x32x16_bf16 v[66:81], v[70:73], v[114:117], 0
	s_cmp_eq_u32 s80, 0
	s_cbranch_scc1 .Lstg_l2
	s_add_i32 s32, s55, -2
	s_cmp_ge_u32 s32, s95
	s_cbranch_scc1 .Lstg_l2
	s_mov_b32 m0, s81
	s_add_u32 s98, s76, 0x1ec08000
	s_addc_u32 s99, s77, 0
	global_load_lds_dwordx4 v0, s[98:99]
	s_mov_b32 m0, s82
	s_add_u32 s98, s78, 0xdc01000
	s_addc_u32 s99, s79, 0
	global_load_lds_dwordx4 v232, s[98:99]
	s_mov_b32 m0, s84
	s_add_u32 s98, s98, 0x80
	s_addc_u32 s99, s99, 0
	global_load_lds_dwordx4 v232, s[98:99]

; #define DMA_WAIT(last) do { if (last) asm volatile("s_waitcnt vmcnt(0)" ::: "memory"); else asm volatile("s_waitcnt vmcnt(%0)" :: "n"(NPW) : "memory"); } while (0)
; template <int DK, int DV, bool OFF, class QLoader> ...
;     ...
;   f32x16 pA0, pA1, pB0, pB1; bf16x8 pa0, pa1, pa2, pa3; const int NT = nkeys / KVBLK;
;   DMA_TILE(0, 0); DMA_TILE(1, 1); DMA_WAIT(false); __syncthreads(); if (2 < NT) DMA_TILE(2, 2);
;   qkt<DK>(pA0, pA1, K_lds, qr, r32, hi); partialSM<DK, OFF>(pA0, pA1, negMC);
.LBB0_868:
.LBB0_870:
	s_add_i32 s24, s55, -1
	s_cmp_ge_u32 s24, s95
	s_waitcnt vmcnt(0)
	s_barrier
	s_cbranch_scc1 .LBB0_872
	s_cmp_lg_u32 s80, 0
	s_cbranch_scc1 .LBB0_872
	s_mov_b32 m0, s85
	s_add_u32 s98, s76, 0x1ec0a000
	s_addc_u32 s99, s77, 0
	global_load_lds_dwordx4 v0, s[98:99]
	s_mov_b32 m0, s87
	s_add_u32 s98, s78, 0xdc61000
	s_addc_u32 s99, s79, 0
	global_load_lds_dwordx4 v232, s[98:99]
	s_mov_b32 m0, s88
	s_add_u32 s98, s98, 0x80
	s_addc_u32 s99, s99, 0
	global_load_lds_dwordx4 v232, s[98:99]
.LBB0_872:
	ds_read_b128 v[82:85], v162 offset:49152
	ds_read_b128 v[86:89], v162 offset:53248
	ds_read_b128 v[130:133], v164 offset:49152
	ds_read_b128 v[134:137], v164 offset:53248
	v_exp_f32_e32 v66, v66
	v_add_f32_e32 v180, 0, v173
	v_add_f32_e32 v180, v174, v180
	v_add_f32_e32 v180, v175, v180
	v_add_f32_e32 v180, v184, v180
	v_add_f32_e32 v180, v185, v180
	v_add_f32_e32 v180, v186, v180
	v_add_f32_e32 v180, v187, v180
	v_add_f32_e32 v180, v188, v180
	v_add_f32_e32 v180, v189, v180
	v_add_f32_e32 v180, v190, v180
	v_add_f32_e32 v180, v191, v180
	v_add_f32_e32 v180, v192, v180
	v_add_f32_e32 v180, v193, v180
	v_add_f32_e32 v180, v194, v180
	v_add_f32_e32 v180, v195, v180
	v_add_f32_e32 v180, v196, v180
	s_waitcnt lgkmcnt(0)
	v_mfma_f32_32x32x16_bf16 v[98:113], v[82:85], v[114:117], 0
	v_exp_f32_e32 v67, v67
	v_exp_f32_e32 v68, v68
	v_exp_f32_e32 v69, v69
	v_exp_f32_e32 v70, v70
	v_exp_f32_e32 v71, v71
	v_exp_f32_e32 v72, v72
	v_exp_f32_e32 v73, v73
	v_mfma_f32_32x32x16_bf16 v[82:97], v[86:89], v[114:117], 0
	s_cmp_eq_u32 s80, 0
	s_cbranch_scc1 .Lstg_l3
	s_add_i32 s32, s55, -1
	s_cmp_ge_u32 s32, s95
	s_cbranch_scc1 .Lstg_l3
	s_mov_b32 m0, s85
	s_add_u32 s98, s76, 0x1ec0a000
	s_addc_u32 s99, s77, 0
	global_load_lds_dwordx4 v0, s[98:99]
	s_mov_b32 m0, s87
	s_add_u32 s98, s78, 0xdc61000
	s_addc_u32 s99, s79, 0
	global_load_lds_dwordx4 v232, s[98:99]
	s_mov_b32 m0, s88
	s_add_u32 s98, s98, 0x80
	s_addc_u32 s99, s99, 0
	global_load_lds_dwordx4 v232, s[98:99]

; #define DMA_WAIT(last) do { if (last) asm volatile("s_waitcnt vmcnt(0)" ::: "memory"); else asm volatile("s_waitcnt vmcnt(%0)" :: "n"(NPW) : "memory"); } while (0)
; template <int DK, int DV, bool OFF, class QLoader> ...
;     ...
;   f32x16 pA0, pA1, pB0, pB1; bf16x8 pa0, pa1, pa2, pa3; const int NT = nkeys / KVBLK;
;   DMA_TILE(0, 0); DMA_TILE(1, 1); DMA_WAIT(false); __syncthreads(); if (2 < NT) DMA_TILE(2, 2);
;   qkt<DK>(pA0, pA1, K_lds, qr, r32, hi); partialSM<DK, OFF>(pA0, pA1, negMC);
.LBB0_875:
.LBB0_877:
	s_cmp_ge_u32 s55, s95
	s_waitcnt vmcnt(0)
	s_barrier
	s_cbranch_scc1 .LBB0_879
	s_cmp_lg_u32 s80, 0
	s_cbranch_scc1 .LBB0_879
	s_mov_b32 m0, s89
	s_add_u32 s98, s76, 0x1ec0c000
	s_addc_u32 s99, s77, 0
	global_load_lds_dwordx4 v0, s[98:99]
	s_mov_b32 m0, s91
	s_add_u32 s98, s78, 0xdcc1000
	s_addc_u32 s99, s79, 0
	global_load_lds_dwordx4 v232, s[98:99]
	s_mov_b32 m0, s92
	s_add_u32 s98, s98, 0x80
	s_addc_u32 s99, s99, 0
	global_load_lds_dwordx4 v232, s[98:99]
.LBB0_879:
	ds_read_b128 v[66:69], v162
	ds_read_b128 v[70:73], v162 offset:4096
	ds_read_b128 v[130:133], v164
	ds_read_b128 v[134:137], v164 offset:4096
	v_exp_f32_e32 v82, v82
	v_exp_f32_e32 v83, v83
	v_add_f32_e32 v180, 0, v197
	v_add_f32_e32 v180, v200, v180
	v_add_f32_e32 v180, v198, v180
	v_add_f32_e32 v180, v202, v180
	v_add_f32_e32 v180, v204, v180
	v_add_f32_e32 v180, v207, v180
	v_add_f32_e32 v180, v205, v180
	v_add_f32_e32 v180, v210, v180
	v_add_f32_e32 v180, v199, v180
	v_add_f32_e32 v180, v203, v180
	v_add_f32_e32 v180, v201, v180
	v_add_f32_e32 v180, v209, v180
	v_add_f32_e32 v180, v206, v180
	v_add_f32_e32 v180, v211, v180
	v_add_f32_e32 v180, v208, v180
	v_add_f32_e32 v180, v212, v180
	s_waitcnt lgkmcnt(0)
	v_mfma_f32_32x32x16_bf16 v[98:113], v[66:69], v[114:117], 0
	v_exp_f32_e32 v84, v84
	v_exp_f32_e32 v85, v85
	v_exp_f32_e32 v86, v86
	v_exp_f32_e32 v87, v87
	v_exp_f32_e32 v88, v88
	v_exp_f32_e32 v89, v89
	v_exp_f32_e32 v90, v90
	v_mfma_f32_32x32x16_bf16 v[66:81], v[70:73], v[114:117], 0
	s_cmp_eq_u32 s80, 0
	s_cbranch_scc1 .Lstg_l4
	s_cmp_ge_u32 s55, s95
	s_cbranch_scc1 .Lstg_l4
	s_mov_b32 m0, s89
	s_add_u32 s98, s76, 0x1ec0c000
	s_addc_u32 s99, s77, 0
	global_load_lds_dwordx4 v0, s[98:99]
	s_mov_b32 m0, s91
	s_add_u32 s98, s78, 0xdcc1000
	s_addc_u32 s99, s79, 0
	global_load_lds_dwordx4 v232, s[98:99]
	s_mov_b32 m0, s92
	s_add_u32 s98, s98, 0x80
	s_addc_u32 s99, s99, 0
	global_load_lds_dwordx4 v232, s[98:99]
